# s20 + 2688 MoE conversion items moved from P0 (HBM-bound) into the P3|P4 seam's idle window of workgroups 64.. (3 items per wave there instead of 1)
# speedup vs baseline: 1.0044x; 1.0044x over previous
; __device__ __forceinline__ void item8_load(const float* W, int N, int k0, int n0, int lane, f32x4 (&rg)[16]) {
; #pragma unroll
;     for (int i = 0; i < 16; ++i) rg[i] = __builtin_nontemporal_load((const f32x4*)(W + (size_t)(k0 + 8 * i + (lane >> 3)) * N + n0 + 4 * (lane & 7)));
; }
.LBB0_70:
	s_cmpk_lt_i32 s50, 0x40
	s_cbranch_scc0 .LBB0_72
	s_ashr_i32 s0, s50, 31
	s_lshr_b32 s0, s0, 21
	s_add_i32 s1, s50, s0
	s_ashr_i32 s0, s1, 11
	s_and_b32 s1, s1, 0xf800
	s_sub_i32 s3, s50, s1
	s_ashr_i32 s1, s0, 31
	s_lshl_b64 s[0:1], s[0:1], 25
	s_add_u32 s4, s66, s0
	s_sext_i32_i16 s0, s3
	s_addc_u32 s5, s67, s1
	s_bfe_u32 s0, s0, 0x70018
	s_add_i32 s0, s3, s0
	s_sext_i32_i16 s1, s0
	s_and_b32 s0, s0, 0xff80
	s_sub_i32 s0, s3, s0
	s_sext_i32_i16 s0, s0
	s_and_b32 s1, s1, 0xffffff80
	s_lshl_b32 s0, s0, 5
	v_or_b32_e32 v50, s1, v1
	s_ashr_i32 s1, s0, 31
	s_lshl_b64 s[0:1], s[0:1], 2
	s_add_u32 s0, s4, s0
	s_waitcnt vmcnt(10)
	v_or_b32_e32 v4, 8, v50
	s_waitcnt vmcnt(8)
	v_or_b32_e32 v10, 16, v50
	v_or_b32_e32 v12, 24, v50
	s_waitcnt vmcnt(6)
	v_or_b32_e32 v18, 32, v50
	v_or_b32_e32 v20, 40, v50
	s_waitcnt vmcnt(4)
	v_or_b32_e32 v26, 48, v50
	v_or_b32_e32 v28, 56, v50
	v_or_b32_e32 v34, 64, v50
	v_or_b32_e32 v36, 0x48, v50
	v_or_b32_e32 v42, 0x50, v50
	v_or_b32_e32 v44, 0x58, v50
	v_or_b32_e32 v54, 0x60, v50
	s_addc_u32 s1, s5, s1
	v_mov_b32_e32 v131, 0
	v_ashrrev_i32_e32 v51, 31, v50
	v_ashrrev_i32_e32 v5, 31, v4
	v_ashrrev_i32_e32 v11, 31, v10
	v_ashrrev_i32_e32 v13, 31, v12
	v_ashrrev_i32_e32 v19, 31, v18
	v_ashrrev_i32_e32 v21, 31, v20
	v_ashrrev_i32_e32 v27, 31, v26
	v_ashrrev_i32_e32 v29, 31, v28
	v_ashrrev_i32_e32 v35, 31, v34
	v_ashrrev_i32_e32 v37, 31, v36
	v_ashrrev_i32_e32 v43, 31, v42
	v_ashrrev_i32_e32 v45, 31, v44
	v_ashrrev_i32_e32 v55, 31, v54
	v_or_b32_e32 v56, 0x68, v50
	v_lshl_add_u64 v[52:53], s[0:1], 0, v[130:131]
	v_lshlrev_b64 v[2:3], 14, v[50:51]
	v_lshlrev_b64 v[4:5], 14, v[4:5]
	v_lshlrev_b64 v[10:11], 14, v[10:11]
	v_lshlrev_b64 v[12:13], 14, v[12:13]
	v_lshlrev_b64 v[18:19], 14, v[18:19]
	v_lshlrev_b64 v[20:21], 14, v[20:21]
	v_lshlrev_b64 v[26:27], 14, v[26:27]
	v_lshlrev_b64 v[28:29], 14, v[28:29]
	v_lshlrev_b64 v[34:35], 14, v[34:35]
	v_lshlrev_b64 v[36:37], 14, v[36:37]
	v_lshlrev_b64 v[42:43], 14, v[42:43]
	v_lshlrev_b64 v[44:45], 14, v[44:45]
	v_lshlrev_b64 v[54:55], 14, v[54:55]
	v_ashrrev_i32_e32 v57, 31, v56
	v_lshl_add_u64 v[2:3], v[52:53], 0, v[2:3]
	v_lshl_add_u64 v[6:7], v[52:53], 0, v[4:5]
	v_lshl_add_u64 v[10:11], v[52:53], 0, v[10:11]
	v_lshl_add_u64 v[14:15], v[52:53], 0, v[12:13]
	v_lshl_add_u64 v[18:19], v[52:53], 0, v[18:19]
	v_lshl_add_u64 v[22:23], v[52:53], 0, v[20:21]
	v_lshl_add_u64 v[26:27], v[52:53], 0, v[26:27]
	v_lshl_add_u64 v[30:31], v[52:53], 0, v[28:29]
	v_lshl_add_u64 v[34:35], v[52:53], 0, v[34:35]
	v_lshl_add_u64 v[38:39], v[52:53], 0, v[36:37]
	v_lshl_add_u64 v[42:43], v[52:53], 0, v[42:43]
	v_lshl_add_u64 v[46:47], v[52:53], 0, v[44:45]
	v_lshl_add_u64 v[54:55], v[52:53], 0, v[54:55]
	v_lshlrev_b64 v[56:57], 14, v[56:57]
	global_load_dwordx4 v[2:5], v[2:3], off nt
	s_nop 0
	global_load_dwordx4 v[6:9], v[6:7], off nt
	s_nop 0
	global_load_dwordx4 v[10:13], v[10:11], off nt
	s_nop 0
	global_load_dwordx4 v[14:17], v[14:15], off nt
	s_nop 0
	global_load_dwordx4 v[18:21], v[18:19], off nt
	s_nop 0
	global_load_dwordx4 v[22:25], v[22:23], off nt
	s_nop 0
	global_load_dwordx4 v[26:29], v[26:27], off nt
	s_nop 0
	global_load_dwordx4 v[30:33], v[30:31], off nt
	s_nop 0
	global_load_dwordx4 v[34:37], v[34:35], off nt
	s_nop 0
	global_load_dwordx4 v[38:41], v[38:39], off nt
	s_nop 0
	global_load_dwordx4 v[42:45], v[42:43], off nt
	s_nop 0
	global_load_dwordx4 v[46:49], v[46:47], off nt
	v_lshl_add_u64 v[56:57], v[52:53], 0, v[56:57]
	global_load_dwordx4 v[66:69], v[54:55], off nt
	global_load_dwordx4 v[70:73], v[56:57], off nt
	v_or_b32_e32 v54, 0x70, v50
	v_ashrrev_i32_e32 v55, 31, v54
	v_or_b32_e32 v50, 0x78, v50
	v_lshlrev_b64 v[54:55], 14, v[54:55]
	v_ashrrev_i32_e32 v51, 31, v50
	v_lshl_add_u64 v[54:55], v[52:53], 0, v[54:55]
	v_lshlrev_b64 v[50:51], 14, v[50:51]
	v_lshl_add_u64 v[50:51], v[52:53], 0, v[50:51]
	global_load_dwordx4 v[90:93], v[54:55], off nt
	global_load_dwordx4 v[94:97], v[50:51], off nt

.LBB0_75:
	s_cmpk_gt_i32 s2, 0x3f
	s_mov_b64 s[0:1], -1
	s_cbranch_scc1 .LBB0_74
	s_add_i32 s3, s2, s92
	s_cmpk_lt_i32 s3, 0x40
	s_cselect_b64 s[4:5], -1, 0
	s_cmpk_gt_i32 s3, 0x3f
	s_cselect_b64 s[0:1], -1, 0
	s_and_b64 vcc, exec, s[0:1]
	s_cbranch_vccnz .LBB0_78
	s_ashr_i32 s6, s3, 31
	s_lshr_b32 s6, s6, 21
	s_add_i32 s6, s3, s6
	s_and_b32 s7, s6, 0xf800
	s_ashr_i32 s6, s6, 11
	s_sub_i32 s8, s3, s7
	s_ashr_i32 s7, s6, 31
	s_lshl_b64 s[6:7], s[6:7], 25
	s_add_u32 s9, s66, s6
	s_sext_i32_i16 s6, s8
	s_addc_u32 s10, s67, s7
	s_bfe_u32 s6, s6, 0x70018
	s_add_i32 s6, s8, s6
	s_sext_i32_i16 s7, s6
	s_and_b32 s6, s6, 0xff80
	s_sub_i32 s6, s8, s6
	s_sext_i32_i16 s6, s6
	s_and_b32 s7, s7, 0xffffff80
	s_lshl_b32 s6, s6, 5
	v_or_b32_e32 v122, s7, v1
	s_ashr_i32 s7, s6, 31
	s_lshl_b64 s[6:7], s[6:7], 2
	v_ashrrev_i32_e32 v123, 31, v122
	s_add_u32 s6, s9, s6
	v_lshlrev_b64 v[50:51], 14, v[122:123]
	v_or_b32_e32 v52, 8, v122
	v_or_b32_e32 v58, 16, v122
	v_or_b32_e32 v60, 24, v122
	v_or_b32_e32 v74, 32, v122
	v_or_b32_e32 v76, 40, v122
	v_or_b32_e32 v82, 48, v122
	v_or_b32_e32 v84, 56, v122
	v_or_b32_e32 v98, 64, v122
	v_or_b32_e32 v100, 0x48, v122
	v_or_b32_e32 v106, 0x50, v122
	v_or_b32_e32 v108, 0x58, v122
	v_or_b32_e32 v114, 0x60, v122
	v_or_b32_e32 v116, 0x68, v122
	v_or_b32_e32 v126, 0x70, v122
	v_or_b32_e32 v122, 0x78, v122
	s_addc_u32 s7, s10, s7
	v_ashrrev_i32_e32 v53, 31, v52
	v_ashrrev_i32_e32 v59, 31, v58
	v_ashrrev_i32_e32 v61, 31, v60
	v_ashrrev_i32_e32 v75, 31, v74
	v_ashrrev_i32_e32 v77, 31, v76
	v_ashrrev_i32_e32 v83, 31, v82
	v_ashrrev_i32_e32 v85, 31, v84
	v_ashrrev_i32_e32 v99, 31, v98
	v_ashrrev_i32_e32 v101, 31, v100
	v_ashrrev_i32_e32 v107, 31, v106
	v_ashrrev_i32_e32 v109, 31, v108
	v_ashrrev_i32_e32 v115, 31, v114
	v_ashrrev_i32_e32 v117, 31, v116
	v_ashrrev_i32_e32 v127, 31, v126
	v_ashrrev_i32_e32 v123, 31, v122
	v_lshl_add_u64 v[124:125], s[6:7], 0, v[130:131]
	v_lshlrev_b64 v[52:53], 14, v[52:53]
	v_lshlrev_b64 v[58:59], 14, v[58:59]
	v_lshlrev_b64 v[60:61], 14, v[60:61]
	v_lshlrev_b64 v[74:75], 14, v[74:75]
	v_lshlrev_b64 v[76:77], 14, v[76:77]
	v_lshlrev_b64 v[82:83], 14, v[82:83]
	v_lshlrev_b64 v[84:85], 14, v[84:85]
	v_lshlrev_b64 v[98:99], 14, v[98:99]
	v_lshlrev_b64 v[100:101], 14, v[100:101]
	v_lshlrev_b64 v[106:107], 14, v[106:107]
	v_lshlrev_b64 v[108:109], 14, v[108:109]
	v_lshlrev_b64 v[114:115], 14, v[114:115]
	v_lshlrev_b64 v[116:117], 14, v[116:117]
	v_lshlrev_b64 v[126:127], 14, v[126:127]
	v_lshlrev_b64 v[122:123], 14, v[122:123]
	v_lshl_add_u64 v[50:51], v[124:125], 0, v[50:51]
	v_lshl_add_u64 v[54:55], v[124:125], 0, v[52:53]
	v_lshl_add_u64 v[58:59], v[124:125], 0, v[58:59]
	v_lshl_add_u64 v[62:63], v[124:125], 0, v[60:61]
	v_lshl_add_u64 v[74:75], v[124:125], 0, v[74:75]
	v_lshl_add_u64 v[78:79], v[124:125], 0, v[76:77]
	v_lshl_add_u64 v[82:83], v[124:125], 0, v[82:83]
	v_lshl_add_u64 v[86:87], v[124:125], 0, v[84:85]
	v_lshl_add_u64 v[98:99], v[124:125], 0, v[98:99]
	v_lshl_add_u64 v[102:103], v[124:125], 0, v[100:101]
	v_lshl_add_u64 v[106:107], v[124:125], 0, v[106:107]
	v_lshl_add_u64 v[110:111], v[124:125], 0, v[108:109]
	v_lshl_add_u64 v[114:115], v[124:125], 0, v[114:115]
	v_lshl_add_u64 v[118:119], v[124:125], 0, v[116:117]
	v_lshl_add_u64 v[126:127], v[124:125], 0, v[126:127]
	v_lshl_add_u64 v[128:129], v[124:125], 0, v[122:123]
	global_load_dwordx4 v[50:53], v[50:51], off nt
	s_nop 0
	global_load_dwordx4 v[54:57], v[54:55], off nt
	s_nop 0
	global_load_dwordx4 v[58:61], v[58:59], off nt
	s_nop 0
	global_load_dwordx4 v[62:65], v[62:63], off nt
	s_nop 0
	global_load_dwordx4 v[74:77], v[74:75], off nt
	s_nop 0
	global_load_dwordx4 v[78:81], v[78:79], off nt
	s_nop 0
	global_load_dwordx4 v[82:85], v[82:83], off nt
	s_nop 0
	global_load_dwordx4 v[86:89], v[86:87], off nt
	s_nop 0
	global_load_dwordx4 v[98:101], v[98:99], off nt
	s_nop 0
	global_load_dwordx4 v[102:105], v[102:103], off nt
	s_nop 0
	global_load_dwordx4 v[106:109], v[106:107], off nt
	s_nop 0
	global_load_dwordx4 v[110:113], v[110:111], off nt
	s_nop 0
	global_load_dwordx4 v[114:117], v[114:115], off nt
	s_nop 0
	global_load_dwordx4 v[118:121], v[118:119], off nt
	s_nop 0
	global_load_dwordx4 v[122:125], v[126:127], off nt
	s_nop 0
	global_load_dwordx4 v[126:129], v[128:129], off nt
; #define LAS __attribute__((address_space(3)))
; #define LDS_WAIT() asm volatile("s_waitcnt lgkmcnt(0)" ::: "memory")
; __device__ __forceinline__ void item8_finish(int K, unsigned char* WT, int k0, int r0, LAS float* scr, int lane, const f32x4 (&rg)[16]) {
; #pragma unroll
;     for (int i = 0; i < 16; ++i) { LAS float* d = scr + (8 * i + (lane >> 3)) * 33 + 4 * (lane & 7); d[0] = rg[i].x; d[1] = rg[i].y; d[2] = rg[i].z; d[3] = rg[i].w; }
;     LDS_WAIT();
;     const int c = lane & 7;
; #pragma unroll
;     for (int j = 0; j < 4; ++j) { const int n = (lane >> 3) + 8 * j; const LAS float* sp = scr + (16 * c) * 33 + n; int w[4];
; #pragma unroll
;         for (int q = 0; q < 4; ++q) { w[q] = __builtin_amdgcn_cvt_pk_fp8_f32(sp[(4 * q) * 33] * 256.f, sp[(4 * q + 1) * 33] * 256.f, 0, false); w[q] = __builtin_amdgcn_cvt_pk_fp8_f32(sp[(4 * q + 2) * 33] * 256.f, sp[(4 * q + 3) * 33] * 256.f, w[q], true); }
.LBB0_78:
	s_ashr_i32 s6, s2, 31
	s_lshr_b32 s6, s6, 21
	s_add_i32 s7, s2, s6
	v_add_u32_e32 v142, v138, v139
	s_ashr_i32 s6, s7, 11
	s_and_b32 s7, s7, 0xf800
	v_add_u32_e32 v143, 0x420, v142
	v_add_u32_e32 v144, 0x428, v142
	v_add_u32_e32 v145, 0x840, v142
	v_add_u32_e32 v146, 0x848, v142
	v_add_u32_e32 v147, 0xc60, v142
	v_add_u32_e32 v148, 0xc68, v142
	v_add_u32_e32 v149, 0x1080, v142
	v_add_u32_e32 v150, 0x1088, v142
	v_add_u32_e32 v151, 0x14a0, v142
	v_add_u32_e32 v152, 0x14a8, v142
	v_add_u32_e32 v153, 0x18c0, v142
	v_add_u32_e32 v154, 0x18c8, v142
	v_add_u32_e32 v155, 0x1ce0, v142
	v_add_u32_e32 v156, 0x1ce8, v142
	v_add_u32_e32 v157, 0x2100, v142
	v_add_u32_e32 v158, 0x2108, v142
	v_add_u32_e32 v159, 0x2520, v142
	v_add_u32_e32 v160, 0x2528, v142
	v_add_u32_e32 v161, 0x2940, v142
	v_add_u32_e32 v162, 0x2948, v142
	v_add_u32_e32 v163, 0x2d60, v142
	v_add_u32_e32 v164, 0x2d68, v142
	v_add_u32_e32 v165, 0x3180, v142
	v_add_u32_e32 v166, 0x3188, v142
	v_add_u32_e32 v167, 0x35a0, v142
	v_add_u32_e32 v168, 0x35a8, v142
	v_add_u32_e32 v169, 0x39c0, v142
	v_add_u32_e32 v170, 0x39c8, v142
	v_add_u32_e32 v171, 0x3de0, v142
	v_add_u32_e32 v172, 0x3de8, v142
	s_sub_i32 s7, s2, s7
	s_waitcnt vmcnt(10)
	ds_write2_b32 v142, v2, v3 offset1:1
	ds_write2_b32 v142, v4, v5 offset0:2 offset1:3
	ds_write2_b32 v143, v6, v7 offset1:1
	ds_write2_b32 v144, v8, v9 offset1:1
	s_waitcnt vmcnt(8)
	ds_write2_b32 v145, v10, v11 offset1:1
	ds_write2_b32 v146, v12, v13 offset1:1
	ds_write2_b32 v147, v14, v15 offset1:1
	ds_write2_b32 v148, v16, v17 offset1:1
	s_waitcnt vmcnt(6)
	ds_write2_b32 v149, v18, v19 offset1:1
	ds_write2_b32 v150, v20, v21 offset1:1
	ds_write2_b32 v151, v22, v23 offset1:1
	ds_write2_b32 v152, v24, v25 offset1:1
	s_waitcnt vmcnt(4)
	ds_write2_b32 v153, v26, v27 offset1:1
	ds_write2_b32 v154, v28, v29 offset1:1
	ds_write2_b32 v155, v30, v31 offset1:1
	ds_write2_b32 v156, v32, v33 offset1:1
	ds_write2_b32 v157, v34, v35 offset1:1
	ds_write2_b32 v158, v36, v37 offset1:1
	ds_write2_b32 v159, v38, v39 offset1:1
	ds_write2_b32 v160, v40, v41 offset1:1
	ds_write2_b32 v161, v42, v43 offset1:1
	ds_write2_b32 v162, v44, v45 offset1:1
	ds_write2_b32 v163, v46, v47 offset1:1
	ds_write2_b32 v164, v48, v49 offset1:1
	s_waitcnt vmcnt(3)
	ds_write2_b32 v165, v66, v67 offset1:1
	ds_write2_b32 v166, v68, v69 offset1:1
	s_waitcnt vmcnt(2)
	ds_write2_b32 v167, v70, v71 offset1:1
	ds_write2_b32 v168, v72, v73 offset1:1
	s_waitcnt vmcnt(1)
	ds_write2_b32 v169, v90, v91 offset1:1
	ds_write2_b32 v170, v92, v93 offset1:1
	s_waitcnt vmcnt(0)
	ds_write2_b32 v171, v94, v95 offset1:1
	ds_write2_b32 v172, v96, v97 offset1:1
	s_sext_i32_i16 s8, s7
	s_waitcnt lgkmcnt(0)
	s_bfe_u32 s8, s8, 0x70018
	ds_read2_b32 v[178:179], v140 offset1:8
	ds_read2_b32 v[180:181], v140 offset0:33 offset1:41
	s_add_i32 s8, s7, s8
	s_sext_i32_i16 s9, s8
	s_and_b32 s8, s8, 0xff80
	s_sub_i32 s7, s7, s8
	s_bfe_i32 s10, s7, 0x80000
	ds_read2_b32 v[184:185], v140 offset0:66 offset1:74
	ds_read2_b32 v[186:187], v140 offset0:99 offset1:107
	s_bfe_u32 s10, s10, 0x60009
	s_waitcnt lgkmcnt(3)
	v_mul_f32_e32 v141, 0x43800000, v178
	s_waitcnt lgkmcnt(2)
	v_mul_f32_e32 v173, 0x43800000, v180
	v_mov_b32_e32 v174, 0
	ds_read2_b32 v[188:189], v140 offset0:132 offset1:140
	ds_read2_b32 v[190:191], v140 offset0:165 offset1:173
	s_lshl_b32 s8, s7, 5
	s_add_i32 s7, s7, s10
	v_cvt_pk_fp8_f32 v174, v141, v173
	s_bfe_i32 s7, s7, 0x80000
	s_sext_i32_i16 s10, s7
	s_sext_i32_i16 s7, s8
	s_bfe_u32 s7, s7, 0xb0014
	s_waitcnt lgkmcnt(3)
	v_mul_f32_e32 v141, 0x43800000, v184
	s_waitcnt lgkmcnt(2)
	v_mul_f32_e32 v173, 0x43800000, v186
	s_add_i32 s7, s8, s7
	v_cvt_pk_fp8_f32 v174, v141, v173 op_sel:[0,0,1]
	s_waitcnt lgkmcnt(1)
	v_mul_f32_e32 v141, 0x43800000, v188
	s_waitcnt lgkmcnt(0)
	v_mul_f32_e32 v173, 0x43800000, v190
	v_mov_b32_e32 v175, 0
	s_and_b32 s7, s7, 0xf800
	v_cvt_pk_fp8_f32 v175, v141, v173
	ds_read2_b32 v[192:193], v140 offset0:198 offset1:206
	ds_read2_b32 v[196:197], v140 offset0:231 offset1:239
	v_add_u32_e32 v141, 0x400, v140
	s_sub_i32 s8, s8, s7
	s_ashr_i32 s7, s6, 31
	ds_read2_b32 v[198:199], v141 offset0:8 offset1:16
	ds_read2_b32 v[200:201], v141 offset0:41 offset1:49
	s_lshl_b64 s[6:7], s[6:7], 23
	ds_read2_b32 v[202:203], v141 offset0:74 offset1:82
	ds_read2_b32 v[204:205], v141 offset0:107 offset1:115
	ds_read2_b32 v[206:207], v141 offset0:140 offset1:148
	ds_read2_b32 v[208:209], v141 offset0:173 offset1:181
	s_add_u32 s11, s93, s6
	v_readlane_b32 s6, v246, 22
	s_addc_u32 s7, s6, s7
	s_sext_i32_i16 s6, s8
	s_bfe_u32 s6, s6, 0x70018
	s_waitcnt lgkmcnt(7)
	v_mul_f32_e32 v173, 0x43800000, v192
	s_waitcnt lgkmcnt(6)
	v_mul_f32_e32 v176, 0x43800000, v196
	s_add_i32 s6, s8, s6
	v_cvt_pk_fp8_f32 v175, v173, v176 op_sel:[0,0,1]
	s_waitcnt lgkmcnt(5)
	v_mul_f32_e32 v173, 0x43800000, v198
	s_waitcnt lgkmcnt(4)
	v_mul_f32_e32 v177, 0x43800000, v200
	v_mov_b32_e32 v176, 0
	ds_read2_b32 v[210:211], v141 offset0:206 offset1:214
	ds_read2_b32 v[212:213], v141 offset0:239 offset1:247
	s_sext_i32_i16 s12, s6
	s_and_b32 s6, s6, 0xff80
	v_cvt_pk_fp8_f32 v176, v173, v177
	s_waitcnt lgkmcnt(3)
	v_mul_f32_e32 v180, 0x43800000, v206
	s_waitcnt lgkmcnt(2)
	v_mul_f32_e32 v184, 0x43800000, v208
	v_mov_b32_e32 v177, 0
	s_lshl_b32 s10, s10, 1
	s_sub_i32 s6, s8, s6
	v_cvt_pk_fp8_f32 v177, v180, v184
	s_lshl_b32 s12, s12, 1
	s_and_b32 s10, s10, 0xffffff80
	s_sext_i32_i16 s6, s6
	s_and_b32 s9, s9, 0xffffff80
	s_and_b32 s12, s12, 0xffffff00
	s_add_i32 s6, s10, s6
	v_mul_f32_e32 v173, 0x43800000, v202
	v_mul_f32_e32 v178, 0x43800000, v204
	s_add_i32 s6, s6, s12
	s_ashr_i32 s10, s9, 31
	v_cvt_pk_fp8_f32 v176, v173, v178 op_sel:[0,0,1]
	s_waitcnt lgkmcnt(1)
; #define LAS __attribute__((address_space(3)))
; #define LDS_WAIT() asm volatile("s_waitcnt lgkmcnt(0)" ::: "memory")
; __device__ __forceinline__ void item8_finish(int K, unsigned char* WT, int k0, int r0, LAS float* scr, int lane, const f32x4 (&rg)[16]) {
; #pragma unroll
;     for (int i = 0; i < 16; ++i) { LAS float* d = scr + (8 * i + (lane >> 3)) * 33 + 4 * (lane & 7); d[0] = rg[i].x; d[1] = rg[i].y; d[2] = rg[i].z; d[3] = rg[i].w; }
;     LDS_WAIT();
;     const int c = lane & 7;
; #pragma unroll
;     for (int j = 0; j < 4; ++j) { const int n = (lane >> 3) + 8 * j; const LAS float* sp = scr + (16 * c) * 33 + n; int w[4];
; #pragma unroll
;         for (int q = 0; q < 4; ++q) { w[q] = __builtin_amdgcn_cvt_pk_fp8_f32(sp[(4 * q) * 33] * 256.f, sp[(4 * q + 1) * 33] * 256.f, 0, false); w[q] = __builtin_amdgcn_cvt_pk_fp8_f32(sp[(4 * q + 2) * 33] * 256.f, sp[(4 * q + 3) * 33] * 256.f, w[q], true); }
;         u32x4 o; o.x = (unsigned)w[0]; o.y = (unsigned)w[1]; o.z = (unsigned)w[2]; o.w = (unsigned)w[3];
;         __builtin_nontemporal_store(o, (u32x4*)(WT + (size_t)(r0 + n) * K + k0 + 16 * c)); }
;     LDS_WAIT();
; }
	v_mul_f32_e32 v173, 0x43800000, v210
	s_waitcnt lgkmcnt(0)
	v_mul_f32_e32 v178, 0x43800000, v212
	s_add_u32 s8, s11, s9
	v_cvt_pk_fp8_f32 v177, v173, v178 op_sel:[0,0,1]
	v_or_b32_e32 v214, s6, v1
	s_addc_u32 s9, s7, s10
	v_ashrrev_i32_e32 v215, 31, v214
	v_lshl_add_u64 v[182:183], s[8:9], 0, v[132:133]
	v_lshlrev_b64 v[214:215], 11, v[214:215]
	v_lshl_add_u64 v[214:215], v[182:183], 0, v[214:215]
	global_store_dwordx4 v[214:215], v[174:177], off nt
	v_mul_f32_e32 v173, 0x43800000, v179
	v_mul_f32_e32 v178, 0x43800000, v191
	v_mul_f32_e32 v175, 0x43800000, v181
	v_mov_b32_e32 v174, 0
	v_cvt_pk_fp8_f32 v174, v173, v175
	v_mul_f32_e32 v177, 0x43800000, v189
	v_mov_b32_e32 v175, 0
	v_cvt_pk_fp8_f32 v175, v177, v178
	v_mul_f32_e32 v173, 0x43800000, v185
	v_mul_f32_e32 v176, 0x43800000, v187
	v_cvt_pk_fp8_f32 v174, v173, v176 op_sel:[0,0,1]
	v_mul_f32_e32 v173, 0x43800000, v193
	v_mul_f32_e32 v176, 0x43800000, v197
	v_cvt_pk_fp8_f32 v175, v173, v176 op_sel:[0,0,1]
	v_mul_f32_e32 v173, 0x43800000, v199
	v_mul_f32_e32 v177, 0x43800000, v201
	v_mov_b32_e32 v176, 0
	v_cvt_pk_fp8_f32 v176, v173, v177
	v_mul_f32_e32 v179, 0x43800000, v207
	v_mul_f32_e32 v180, 0x43800000, v209
	v_mov_b32_e32 v177, 0
	v_cvt_pk_fp8_f32 v177, v179, v180
	v_mul_f32_e32 v173, 0x43800000, v203
	v_mul_f32_e32 v178, 0x43800000, v205
	v_cvt_pk_fp8_f32 v176, v173, v178 op_sel:[0,0,1]
	v_mul_f32_e32 v173, 0x43800000, v211
	v_mul_f32_e32 v178, 0x43800000, v213
	v_cvt_pk_fp8_f32 v177, v173, v178 op_sel:[0,0,1]
	v_or_b32_e32 v178, s6, v135
	v_ashrrev_i32_e32 v179, 31, v178
	ds_read2_b32 v[180:181], v140 offset0:16 offset1:24
	ds_read2_b32 v[184:185], v140 offset0:49 offset1:57
	v_lshlrev_b64 v[178:179], 11, v[178:179]
	v_lshl_add_u64 v[178:179], v[182:183], 0, v[178:179]
	global_store_dwordx4 v[178:179], v[174:177], off nt
	ds_read2_b32 v[178:179], v140 offset0:82 offset1:90
	ds_read2_b32 v[186:187], v140 offset0:115 offset1:123
	s_waitcnt lgkmcnt(3)
	v_mul_f32_e32 v173, 0x43800000, v180
	s_waitcnt lgkmcnt(2)
	v_mul_f32_e32 v175, 0x43800000, v184
	v_mov_b32_e32 v174, 0
	ds_read2_b32 v[188:189], v140 offset0:148 offset1:156
	ds_read2_b32 v[190:191], v140 offset0:181 offset1:189
	v_cvt_pk_fp8_f32 v174, v173, v175
	s_waitcnt lgkmcnt(3)
	v_mul_f32_e32 v173, 0x43800000, v178
	s_waitcnt lgkmcnt(2)
	v_mul_f32_e32 v175, 0x43800000, v186
	ds_read2_b32 v[192:193], v140 offset0:214 offset1:222
	ds_read2_b32 v[196:197], v140 offset0:247 offset1:255
	v_cvt_pk_fp8_f32 v174, v173, v175 op_sel:[0,0,1]
	s_waitcnt lgkmcnt(3)
	v_mul_f32_e32 v173, 0x43800000, v188
	s_waitcnt lgkmcnt(2)
	v_mul_f32_e32 v176, 0x43800000, v190
	v_mov_b32_e32 v175, 0
	ds_read2_b32 v[198:199], v141 offset0:24 offset1:32
	ds_read2_b32 v[200:201], v141 offset0:57 offset1:65
	v_cvt_pk_fp8_f32 v175, v173, v176
	ds_read2_b32 v[202:203], v141 offset0:90 offset1:98
	ds_read2_b32 v[204:205], v141 offset0:123 offset1:131
	ds_read2_b32 v[206:207], v141 offset0:156 offset1:164
	ds_read2_b32 v[208:209], v141 offset0:189 offset1:197
	s_waitcnt lgkmcnt(7)
	v_mul_f32_e32 v173, 0x43800000, v192
	s_waitcnt lgkmcnt(6)
	v_mul_f32_e32 v176, 0x43800000, v196
	v_cvt_pk_fp8_f32 v175, v173, v176 op_sel:[0,0,1]
	s_waitcnt lgkmcnt(5)
	v_mul_f32_e32 v173, 0x43800000, v198
	s_waitcnt lgkmcnt(4)
	v_mul_f32_e32 v177, 0x43800000, v200
	v_mov_b32_e32 v176, 0
	v_cvt_pk_fp8_f32 v176, v173, v177
	v_add_u32_e32 v173, 0x600, v140
	ds_read2_b32 v[210:211], v141 offset0:222 offset1:230
	ds_read2_b32 v[212:213], v173 offset0:127 offset1:135
	s_waitcnt lgkmcnt(3)
	v_mul_f32_e32 v184, 0x43800000, v206
	s_waitcnt lgkmcnt(2)
	v_mul_f32_e32 v186, 0x43800000, v208
	v_mov_b32_e32 v177, 0
	v_cvt_pk_fp8_f32 v177, v184, v186
	v_mul_f32_e32 v178, 0x43800000, v202
	v_mul_f32_e32 v180, 0x43800000, v204
	v_cvt_pk_fp8_f32 v176, v178, v180 op_sel:[0,0,1]
	s_waitcnt lgkmcnt(1)
	v_mul_f32_e32 v178, 0x43800000, v210
	s_waitcnt lgkmcnt(0)
	v_mul_f32_e32 v180, 0x43800000, v212
	v_cvt_pk_fp8_f32 v177, v178, v180 op_sel:[0,0,1]
	v_or_b32_e32 v214, s6, v136
	v_ashrrev_i32_e32 v215, 31, v214
	v_lshlrev_b64 v[214:215], 11, v[214:215]
	v_lshl_add_u64 v[214:215], v[182:183], 0, v[214:215]
	global_store_dwordx4 v[214:215], v[174:177], off nt
	v_mul_f32_e32 v178, 0x43800000, v189
	v_mul_f32_e32 v180, 0x43800000, v207
	v_mul_f32_e32 v175, 0x43800000, v181
	v_mul_f32_e32 v176, 0x43800000, v185
	v_mov_b32_e32 v174, 0
	v_cvt_pk_fp8_f32 v174, v175, v176
	v_mul_f32_e32 v176, 0x43800000, v179
	v_mul_f32_e32 v179, 0x43800000, v191
	v_mov_b32_e32 v175, 0
	v_cvt_pk_fp8_f32 v175, v178, v179
	v_mul_f32_e32 v177, 0x43800000, v187
	v_cvt_pk_fp8_f32 v174, v176, v177 op_sel:[0,0,1]
	v_mul_f32_e32 v176, 0x43800000, v193
	v_mul_f32_e32 v177, 0x43800000, v197
	v_cvt_pk_fp8_f32 v175, v176, v177 op_sel:[0,0,1]
	v_mul_f32_e32 v177, 0x43800000, v199
	v_mul_f32_e32 v178, 0x43800000, v201
	v_mov_b32_e32 v176, 0
	v_cvt_pk_fp8_f32 v176, v177, v178
	v_mul_f32_e32 v181, 0x43800000, v209
	v_mov_b32_e32 v177, 0
	v_cvt_pk_fp8_f32 v177, v180, v181
	v_mul_f32_e32 v178, 0x43800000, v203
	v_mul_f32_e32 v179, 0x43800000, v205
	v_cvt_pk_fp8_f32 v176, v178, v179 op_sel:[0,0,1]
	v_mul_f32_e32 v178, 0x43800000, v211
	v_mul_f32_e32 v179, 0x43800000, v213
	v_cvt_pk_fp8_f32 v177, v178, v179 op_sel:[0,0,1]
	v_or_b32_e32 v178, s6, v137
	v_ashrrev_i32_e32 v179, 31, v178
	v_lshlrev_b64 v[178:179], 11, v[178:179]
	v_lshl_add_u64 v[178:179], v[182:183], 0, v[178:179]
	global_store_dwordx4 v[178:179], v[174:177], off nt
	s_waitcnt lgkmcnt(0)
	s_andn2_b64 vcc, exec, s[4:5]
	s_cbranch_vccnz .LBB0_74
	s_add_i32 s2, s3, s92
	s_cmpk_gt_i32 s2, 0x3f
	s_cbranch_scc1 .LBB0_73
	s_ashr_i32 s4, s2, 31
	s_lshr_b32 s4, s4, 21
	s_add_i32 s5, s2, s4
	s_ashr_i32 s4, s5, 11
	s_and_b32 s5, s5, 0xf800
	s_sub_i32 s6, s2, s5
	s_ashr_i32 s5, s4, 31
	s_lshl_b64 s[4:5], s[4:5], 25
	s_add_u32 s7, s66, s4
	s_sext_i32_i16 s4, s6
	s_addc_u32 s8, s67, s5
	s_bfe_u32 s4, s4, 0x70018
	s_add_i32 s4, s6, s4
	s_sext_i32_i16 s5, s4
	s_and_b32 s4, s4, 0xff80
	s_sub_i32 s4, s6, s4
	s_sext_i32_i16 s4, s4
	s_and_b32 s5, s5, 0xffffff80
	s_lshl_b32 s4, s4, 5
	v_or_b32_e32 v90, s5, v1
	s_ashr_i32 s5, s4, 31
	s_lshl_b64 s[4:5], s[4:5], 2
	v_ashrrev_i32_e32 v91, 31, v90
	s_add_u32 s4, s7, s4
	v_lshlrev_b64 v[2:3], 14, v[90:91]
	v_or_b32_e32 v4, 8, v90
	v_or_b32_e32 v10, 16, v90
	v_or_b32_e32 v12, 24, v90
	v_or_b32_e32 v18, 32, v90
	v_or_b32_e32 v20, 40, v90
	v_or_b32_e32 v26, 48, v90
	v_or_b32_e32 v28, 56, v90
	v_or_b32_e32 v34, 64, v90
	v_or_b32_e32 v36, 0x48, v90
	v_or_b32_e32 v42, 0x50, v90
	v_or_b32_e32 v44, 0x58, v90
	v_or_b32_e32 v66, 0x60, v90
	v_or_b32_e32 v68, 0x68, v90
	v_or_b32_e32 v94, 0x70, v90
	v_or_b32_e32 v90, 0x78, v90
	s_addc_u32 s5, s8, s5
	v_ashrrev_i32_e32 v5, 31, v4
	v_ashrrev_i32_e32 v11, 31, v10
	v_ashrrev_i32_e32 v13, 31, v12
	v_ashrrev_i32_e32 v19, 31, v18
	v_ashrrev_i32_e32 v21, 31, v20
	v_ashrrev_i32_e32 v27, 31, v26
	v_ashrrev_i32_e32 v29, 31, v28
	v_ashrrev_i32_e32 v35, 31, v34
	v_ashrrev_i32_e32 v37, 31, v36
	v_ashrrev_i32_e32 v43, 31, v42
	v_ashrrev_i32_e32 v45, 31, v44
	v_ashrrev_i32_e32 v67, 31, v66
	v_ashrrev_i32_e32 v69, 31, v68
	v_ashrrev_i32_e32 v95, 31, v94
	v_ashrrev_i32_e32 v91, 31, v90
	v_lshl_add_u64 v[92:93], s[4:5], 0, v[130:131]
	v_lshlrev_b64 v[4:5], 14, v[4:5]
	v_lshlrev_b64 v[10:11], 14, v[10:11]
	v_lshlrev_b64 v[12:13], 14, v[12:13]
	v_lshlrev_b64 v[18:19], 14, v[18:19]
	v_lshlrev_b64 v[20:21], 14, v[20:21]
	v_lshlrev_b64 v[26:27], 14, v[26:27]
	v_lshlrev_b64 v[28:29], 14, v[28:29]
	v_lshlrev_b64 v[34:35], 14, v[34:35]
	v_lshlrev_b64 v[36:37], 14, v[36:37]
	v_lshlrev_b64 v[42:43], 14, v[42:43]
	v_lshlrev_b64 v[44:45], 14, v[44:45]
	v_lshlrev_b64 v[66:67], 14, v[66:67]
	v_lshlrev_b64 v[68:69], 14, v[68:69]
	v_lshlrev_b64 v[94:95], 14, v[94:95]
	v_lshlrev_b64 v[90:91], 14, v[90:91]
	v_lshl_add_u64 v[2:3], v[92:93], 0, v[2:3]
	v_lshl_add_u64 v[6:7], v[92:93], 0, v[4:5]
	v_lshl_add_u64 v[10:11], v[92:93], 0, v[10:11]
	v_lshl_add_u64 v[14:15], v[92:93], 0, v[12:13]
	v_lshl_add_u64 v[18:19], v[92:93], 0, v[18:19]
	v_lshl_add_u64 v[22:23], v[92:93], 0, v[20:21]
	v_lshl_add_u64 v[26:27], v[92:93], 0, v[26:27]
	v_lshl_add_u64 v[30:31], v[92:93], 0, v[28:29]
	v_lshl_add_u64 v[34:35], v[92:93], 0, v[34:35]
	v_lshl_add_u64 v[38:39], v[92:93], 0, v[36:37]
	v_lshl_add_u64 v[42:43], v[92:93], 0, v[42:43]
	v_lshl_add_u64 v[46:47], v[92:93], 0, v[44:45]
	v_lshl_add_u64 v[66:67], v[92:93], 0, v[66:67]
	v_lshl_add_u64 v[70:71], v[92:93], 0, v[68:69]
	v_lshl_add_u64 v[94:95], v[92:93], 0, v[94:95]
	v_lshl_add_u64 v[96:97], v[92:93], 0, v[90:91]
	global_load_dwordx4 v[2:5], v[2:3], off nt
	s_nop 0
	global_load_dwordx4 v[6:9], v[6:7], off nt
	s_nop 0
	global_load_dwordx4 v[10:13], v[10:11], off nt
	s_nop 0
	global_load_dwordx4 v[14:17], v[14:15], off nt
	s_nop 0
	global_load_dwordx4 v[18:21], v[18:19], off nt
	s_nop 0
	global_load_dwordx4 v[22:25], v[22:23], off nt
	s_nop 0
	global_load_dwordx4 v[26:29], v[26:27], off nt
	s_nop 0
	global_load_dwordx4 v[30:33], v[30:31], off nt
	s_nop 0
	global_load_dwordx4 v[34:37], v[34:35], off nt
	s_nop 0
	global_load_dwordx4 v[38:41], v[38:39], off nt
	s_nop 0
	global_load_dwordx4 v[42:45], v[42:43], off nt
	s_nop 0
	global_load_dwordx4 v[46:49], v[46:47], off nt
	s_nop 0
	global_load_dwordx4 v[66:69], v[66:67], off nt
	s_nop 0
	global_load_dwordx4 v[70:73], v[70:71], off nt
	s_nop 0
	global_load_dwordx4 v[90:93], v[94:95], off nt
	s_nop 0
	global_load_dwordx4 v[94:97], v[96:97], off nt
	s_branch .LBB0_73

; #define MOE_LOAD(r_, RG) do { int rr_ = (r_); \
;         if (rr_ < 65536) { const int e_ = rr_ / 2048, q_ = rr_ % 2048; item8_load(w_gu + (size_t)e_ * 2048 * 4096, 4096, 128 * (q_ / 128), 32 * (q_ % 128), lane, RG); } \
;         else { rr_ -= 65536; const int e_ = rr_ / 1024, q_ = rr_ % 1024; item8_load(w_dn + (size_t)e_ * 2048 * 2048, D, 128 * (q_ / 64), 32 * (q_ % 64), lane, RG); } } while (0)
; __global__ void __launch_bounds__(NTHREADS, 2) fwd(Args args) {
;     ...
;     if (IN(3) && IN(4)) xcd_barrier_bg(bar, [&]() {
;         for (int sl_ = bid * 7 + wave - 1; sl_ < CVBG / 6; sl_ += G * 7) { const int it_ = CV_P0 - CVBG + 2 * (CVBG / 6) + sl_; f32x4 rg_[16]; MOE_LOAD(it_, rg_); MOE_FIN(it_, rg_); }
;         if (bid >= 64) for (int sl_ = (bid - 64) * 7 + wave - 1; sl_ < CVSK; sl_ += (G - 64) * 7) { const int it_ = CV_P0 - CVBG - CVSK + sl_; f32x4 rg_[16]; MOE_LOAD(it_, rg_); MOE_FIN(it_, rg_); } });
.LBB0_376:
	s_cmp_gt_i32 s94, 63
	s_cbranch_scc0 .LBB0_380
	s_addk_i32 s2, 0xfe3f
	s_cmpk_gt_i32 s2, 0xfbf
	s_cbranch_scc1 .LBB0_380
	v_readlane_b32 s3, v246, 21
	s_mulk_i32 s3, 0x4200
	v_lshlrev_b32_e32 v5, 4, v0
	v_lshrrev_b32_e32 v22, 3, v220
	v_and_b32_e32 v2, 28, v194
	s_add_i32 s3, s3, 0
	v_and_b32_e32 v18, 0x70, v5
	v_lshl_add_u32 v3, v2, 2, s3
	v_mul_u32_u24_e32 v4, 0x84, v22
	v_mul_u32_u24_e32 v5, 0x84, v18
	v_lshlrev_b32_e32 v6, 2, v22
	v_readlane_b32 s8, v246, 10
	v_mov_b32_e32 v19, 0
	v_add3_u32 v26, s3, v5, v6
	s_mul_i32 s3, s8, 7
	v_add_u32_e32 v27, v3, v4
	v_or_b32_e32 v23, 8, v22
	v_or_b32_e32 v24, 16, v22
	v_or_b32_e32 v25, 24, v22
	s_addk_i32 s3, 0xfe40
	v_lshlrev_b32_e32 v20, 2, v2
	v_mov_b32_e32 v21, v19
	v_add_u32_e32 v28, 0x420, v27
	v_add_u32_e32 v29, 0x428, v27
	v_add_u32_e32 v30, 0x840, v27
	v_add_u32_e32 v31, 0x848, v27
	v_add_u32_e32 v32, 0xc60, v27
	v_add_u32_e32 v33, 0xc68, v27
	v_add_u32_e32 v34, 0x1080, v27
	v_add_u32_e32 v35, 0x1088, v27
	v_add_u32_e32 v36, 0x14a0, v27
	v_add_u32_e32 v37, 0x14a8, v27
	v_add_u32_e32 v38, 0x18c0, v27
	v_add_u32_e32 v39, 0x18c8, v27
	v_add_u32_e32 v40, 0x1ce0, v27
	v_add_u32_e32 v41, 0x1ce8, v27
	v_add_u32_e32 v42, 0x2100, v27
	v_add_u32_e32 v43, 0x2108, v27
	v_add_u32_e32 v44, 0x2520, v27
	v_add_u32_e32 v45, 0x2528, v27
	v_add_u32_e32 v46, 0x2940, v27
	v_add_u32_e32 v47, 0x2948, v27
	v_add_u32_e32 v48, 0x2d60, v27
	v_add_u32_e32 v49, 0x2d68, v27
	v_add_u32_e32 v50, 0x3180, v27
	v_add_u32_e32 v51, 0x3188, v27
	v_add_u32_e32 v52, 0x35a0, v27
	v_add_u32_e32 v53, 0x35a8, v27
	v_add_u32_e32 v54, 0x39c0, v27
	v_add_u32_e32 v55, 0x39c8, v27
	v_add_u32_e32 v56, 0x3de0, v27
	v_add_u32_e32 v57, 0x3de8, v27
	v_add_u32_e32 v58, 0x400, v26
	v_add_u32_e32 v59, 0x600, v26
	v_readlane_b32 s9, v246, 11
.LBB0_379:
	s_add_i32 s8, s2, 0x40
	s_ashr_i32 s9, s8, 31
	s_lshr_b32 s9, s9, 21
	s_add_i32 s9, s8, s9
	s_ashr_i32 s10, s9, 11
	s_and_b32 s9, s9, 0xf800
	s_ashr_i32 s11, s10, 31
	s_sub_i32 s12, s8, s9
	s_lshl_b64 s[8:9], s[10:11], 25
	s_sext_i32_i16 s13, s12
	s_add_u32 s14, s66, s8
	s_addc_u32 s15, s67, s9
	s_bfe_u32 s8, s13, 0x70018
	s_add_i32 s8, s12, s8
	s_sext_i32_i16 s9, s8
	s_and_b32 s8, s8, 0xff80
	s_sub_i32 s17, s12, s8
	s_sext_i32_i16 s18, s17
	s_lshl_b32 s8, s18, 5
	s_and_b32 s16, s9, 0xffffff80
	s_ashr_i32 s9, s8, 31
	v_or_b32_e32 v60, s16, v22
	s_lshl_b64 s[12:13], s[8:9], 2
	v_or_b32_e32 v62, 8, v60
	v_or_b32_e32 v64, 16, v60
	v_or_b32_e32 v66, 24, v60
	v_or_b32_e32 v68, 32, v60
	v_or_b32_e32 v70, 40, v60
	v_or_b32_e32 v72, 48, v60
	v_or_b32_e32 v74, 56, v60
	v_or_b32_e32 v76, 64, v60
	v_or_b32_e32 v78, 0x48, v60
	v_or_b32_e32 v80, 0x50, v60
	v_or_b32_e32 v82, 0x58, v60
	v_or_b32_e32 v84, 0x60, v60
	v_or_b32_e32 v86, 0x68, v60
	v_or_b32_e32 v88, 0x70, v60
	v_or_b32_e32 v90, 0x78, v60
	s_add_u32 s12, s14, s12
	v_ashrrev_i32_e32 v61, 31, v60
	v_ashrrev_i32_e32 v63, 31, v62
	v_ashrrev_i32_e32 v65, 31, v64
	v_ashrrev_i32_e32 v67, 31, v66
	v_ashrrev_i32_e32 v69, 31, v68
	v_ashrrev_i32_e32 v71, 31, v70
	v_ashrrev_i32_e32 v73, 31, v72
	v_ashrrev_i32_e32 v75, 31, v74
	v_ashrrev_i32_e32 v77, 31, v76
	v_ashrrev_i32_e32 v79, 31, v78
	v_ashrrev_i32_e32 v81, 31, v80
	v_ashrrev_i32_e32 v83, 31, v82
	v_ashrrev_i32_e32 v85, 31, v84
	v_ashrrev_i32_e32 v87, 31, v86
	v_ashrrev_i32_e32 v89, 31, v88
	v_ashrrev_i32_e32 v91, 31, v90
	s_addc_u32 s13, s15, s13
	v_lshlrev_b64 v[60:61], 14, v[60:61]
	v_lshlrev_b64 v[62:63], 14, v[62:63]
	v_lshlrev_b64 v[64:65], 14, v[64:65]
	v_lshlrev_b64 v[66:67], 14, v[66:67]
	v_lshlrev_b64 v[68:69], 14, v[68:69]
	v_lshlrev_b64 v[70:71], 14, v[70:71]
	v_lshlrev_b64 v[72:73], 14, v[72:73]
	v_lshlrev_b64 v[74:75], 14, v[74:75]
	v_lshlrev_b64 v[76:77], 14, v[76:77]
	v_lshlrev_b64 v[78:79], 14, v[78:79]
	v_lshlrev_b64 v[80:81], 14, v[80:81]
	v_lshlrev_b64 v[82:83], 14, v[82:83]
	v_lshlrev_b64 v[84:85], 14, v[84:85]
	v_lshlrev_b64 v[86:87], 14, v[86:87]
	v_lshlrev_b64 v[88:89], 14, v[88:89]
	v_lshlrev_b64 v[90:91], 14, v[90:91]
	v_lshl_add_u64 v[92:93], s[12:13], 0, v[20:21]
	v_lshl_add_u64 v[60:61], v[92:93], 0, v[60:61]
	v_lshl_add_u64 v[94:95], v[92:93], 0, v[62:63]
	v_lshl_add_u64 v[96:97], v[92:93], 0, v[64:65]
	v_lshl_add_u64 v[98:99], v[92:93], 0, v[66:67]
	v_lshl_add_u64 v[100:101], v[92:93], 0, v[68:69]
	v_lshl_add_u64 v[102:103], v[92:93], 0, v[70:71]
	v_lshl_add_u64 v[104:105], v[92:93], 0, v[72:73]
	v_lshl_add_u64 v[106:107], v[92:93], 0, v[74:75]
	v_lshl_add_u64 v[108:109], v[92:93], 0, v[76:77]
	v_lshl_add_u64 v[110:111], v[92:93], 0, v[78:79]
	v_lshl_add_u64 v[112:113], v[92:93], 0, v[80:81]
	v_lshl_add_u64 v[114:115], v[92:93], 0, v[82:83]
	v_lshl_add_u64 v[116:117], v[92:93], 0, v[84:85]
	v_lshl_add_u64 v[118:119], v[92:93], 0, v[86:87]
	v_lshl_add_u64 v[120:121], v[92:93], 0, v[88:89]
	v_lshl_add_u64 v[122:123], v[92:93], 0, v[90:91]
	global_load_dwordx4 v[60:63], v[60:61], off nt
	s_nop 0
	global_load_dwordx4 v[64:67], v[94:95], off nt
	global_load_dwordx4 v[68:71], v[96:97], off nt
	global_load_dwordx4 v[72:75], v[98:99], off nt
	global_load_dwordx4 v[76:79], v[100:101], off nt
	global_load_dwordx4 v[80:83], v[102:103], off nt
	global_load_dwordx4 v[84:87], v[104:105], off nt
	global_load_dwordx4 v[88:91], v[106:107], off nt
	global_load_dwordx4 v[92:95], v[108:109], off nt
	global_load_dwordx4 v[96:99], v[110:111], off nt
	s_nop 0
	global_load_dwordx4 v[100:103], v[112:113], off nt
	global_load_dwordx4 v[104:107], v[114:115], off nt
	global_load_dwordx4 v[108:111], v[116:117], off nt
	s_nop 0
	global_load_dwordx4 v[112:115], v[118:119], off nt
	s_nop 0
	global_load_dwordx4 v[116:119], v[120:121], off nt
	s_nop 0
	global_load_dwordx4 v[120:123], v[122:123], off nt
	s_bfe_i32 s9, s17, 0x80000
	s_bfe_u32 s14, s18, 0xb000f
	s_bfe_u32 s9, s9, 0x60009
	s_add_i32 s12, s8, s14
	s_add_i32 s17, s17, s9
	s_and_b32 s9, s12, 0xf800
	s_lshl_b64 s[10:11], s[10:11], 23
	s_bfe_i32 s12, s17, 0x80000
	s_sub_i32 s8, s8, s9
	s_sext_i32_i16 s9, s12
	s_add_u32 s10, s93, s10
	s_sext_i32_i16 s12, s8
	s_waitcnt vmcnt(15)
; #define LAS __attribute__((address_space(3)))
; #define LDS_WAIT() asm volatile("s_waitcnt lgkmcnt(0)" ::: "memory")
; __device__ __forceinline__ void item8_finish(int K, unsigned char* WT, int k0, int r0, LAS float* scr, int lane, const f32x4 (&rg)[16]) {
; #pragma unroll
;     for (int i = 0; i < 16; ++i) { LAS float* d = scr + (8 * i + (lane >> 3)) * 33 + 4 * (lane & 7); d[0] = rg[i].x; d[1] = rg[i].y; d[2] = rg[i].z; d[3] = rg[i].w; }
;     LDS_WAIT();
;     const int c = lane & 7;
; #pragma unroll
;     for (int j = 0; j < 4; ++j) { const int n = (lane >> 3) + 8 * j; const LAS float* sp = scr + (16 * c) * 33 + n; int w[4];
; #pragma unroll
;         for (int q = 0; q < 4; ++q) { w[q] = __builtin_amdgcn_cvt_pk_fp8_f32(sp[(4 * q) * 33] * 256.f, sp[(4 * q + 1) * 33] * 256.f, 0, false); w[q] = __builtin_amdgcn_cvt_pk_fp8_f32(sp[(4 * q + 2) * 33] * 256.f, sp[(4 * q + 3) * 33] * 256.f, w[q], true); }
	ds_write2_b32 v27, v60, v61 offset1:1
	ds_write2_b32 v27, v62, v63 offset0:2 offset1:3
	s_waitcnt vmcnt(14)
	ds_write2_b32 v28, v64, v65 offset1:1
	ds_write2_b32 v29, v66, v67 offset1:1
	s_waitcnt vmcnt(13)
	ds_write2_b32 v30, v68, v69 offset1:1
	ds_write2_b32 v31, v70, v71 offset1:1
	s_waitcnt vmcnt(12)
	ds_write2_b32 v32, v72, v73 offset1:1
	ds_write2_b32 v33, v74, v75 offset1:1
	s_waitcnt vmcnt(11)
	ds_write2_b32 v34, v76, v77 offset1:1
	ds_write2_b32 v35, v78, v79 offset1:1
	s_waitcnt vmcnt(10)
	ds_write2_b32 v36, v80, v81 offset1:1
	ds_write2_b32 v37, v82, v83 offset1:1
	s_waitcnt vmcnt(9)
	ds_write2_b32 v38, v84, v85 offset1:1
	ds_write2_b32 v39, v86, v87 offset1:1
	s_waitcnt vmcnt(8)
	ds_write2_b32 v40, v88, v89 offset1:1
	ds_write2_b32 v41, v90, v91 offset1:1
	s_waitcnt vmcnt(7)
	ds_write2_b32 v42, v92, v93 offset1:1
	ds_write2_b32 v43, v94, v95 offset1:1
	s_waitcnt vmcnt(6)
	ds_write2_b32 v44, v96, v97 offset1:1
	ds_write2_b32 v45, v98, v99 offset1:1
	s_waitcnt vmcnt(5)
	ds_write2_b32 v46, v100, v101 offset1:1
	ds_write2_b32 v47, v102, v103 offset1:1
	s_waitcnt vmcnt(4)
	ds_write2_b32 v48, v104, v105 offset1:1
	ds_write2_b32 v49, v106, v107 offset1:1
	s_waitcnt vmcnt(3)
	ds_write2_b32 v50, v108, v109 offset1:1
	ds_write2_b32 v51, v110, v111 offset1:1
	s_waitcnt vmcnt(2)
	ds_write2_b32 v52, v112, v113 offset1:1
	ds_write2_b32 v53, v114, v115 offset1:1
	s_waitcnt vmcnt(1)
	ds_write2_b32 v54, v116, v117 offset1:1
	ds_write2_b32 v55, v118, v119 offset1:1
	s_waitcnt vmcnt(0)
	ds_write2_b32 v56, v120, v121 offset1:1
	ds_write2_b32 v57, v122, v123 offset1:1
	s_addc_u32 s11, s79, s11
	s_bfe_u32 s12, s12, 0x70018
	s_waitcnt lgkmcnt(0)
	s_add_i32 s12, s8, s12
	ds_read2_b32 v[60:61], v26 offset1:8
	ds_read2_b32 v[62:63], v26 offset0:33 offset1:41
	ds_read2_b32 v[64:65], v26 offset0:66 offset1:74
	ds_read2_b32 v[66:67], v26 offset0:99 offset1:107
	ds_read2_b32 v[68:69], v26 offset0:132 offset1:140
	ds_read2_b32 v[70:71], v26 offset0:165 offset1:173
	ds_read2_b32 v[72:73], v26 offset0:198 offset1:206
	ds_read2_b32 v[74:75], v26 offset0:231 offset1:239
	ds_read2_b32 v[76:77], v58 offset0:8 offset1:16
	ds_read2_b32 v[78:79], v58 offset0:41 offset1:49
	ds_read2_b32 v[80:81], v58 offset0:74 offset1:82
	ds_read2_b32 v[82:83], v58 offset0:107 offset1:115
	ds_read2_b32 v[84:85], v58 offset0:140 offset1:148
	ds_read2_b32 v[86:87], v58 offset0:173 offset1:181
	ds_read2_b32 v[88:89], v58 offset0:206 offset1:214
	ds_read2_b32 v[90:91], v58 offset0:239 offset1:247
	ds_read2_b32 v[92:93], v26 offset0:16 offset1:24
	ds_read2_b32 v[94:95], v26 offset0:49 offset1:57
	ds_read2_b32 v[96:97], v26 offset0:82 offset1:90
	ds_read2_b32 v[98:99], v26 offset0:115 offset1:123
	ds_read2_b32 v[100:101], v26 offset0:148 offset1:156
	ds_read2_b32 v[102:103], v26 offset0:181 offset1:189
	ds_read2_b32 v[104:105], v26 offset0:214 offset1:222
	ds_read2_b32 v[106:107], v26 offset0:247 offset1:255
	ds_read2_b32 v[108:109], v58 offset0:24 offset1:32
	ds_read2_b32 v[110:111], v58 offset0:57 offset1:65
	ds_read2_b32 v[112:113], v58 offset0:90 offset1:98
	ds_read2_b32 v[114:115], v58 offset0:123 offset1:131
	ds_read2_b32 v[116:117], v58 offset0:156 offset1:164
	ds_read2_b32 v[118:119], v58 offset0:189 offset1:197
	ds_read2_b32 v[120:121], v58 offset0:222 offset1:230
	ds_read2_b32 v[122:123], v59 offset0:127 offset1:135
	v_mov_b32_e32 v2, 0
	v_mov_b32_e32 v3, 0
	v_mov_b32_e32 v4, 0
	v_mov_b32_e32 v5, 0
	s_sext_i32_i16 s14, s12
	s_and_b32 s12, s12, 0xff80
	s_waitcnt lgkmcnt(14)
	v_mul_f32_e32 v60, 0x43800000, v60
	v_mul_f32_e32 v62, 0x43800000, v62
	v_mul_f32_e32 v68, 0x43800000, v68
	v_mul_f32_e32 v70, 0x43800000, v70
	v_mul_f32_e32 v76, 0x43800000, v76
	v_mul_f32_e32 v78, 0x43800000, v78
	v_mul_f32_e32 v84, 0x43800000, v84
	v_mul_f32_e32 v86, 0x43800000, v86
	v_mov_b32_e32 v6, 0
	v_mov_b32_e32 v7, 0
	v_mov_b32_e32 v8, 0
	v_mov_b32_e32 v9, 0
	s_lshl_b32 s9, s9, 1
	s_sub_i32 s8, s8, s12
	v_mul_f32_e32 v61, 0x43800000, v61
	v_mul_f32_e32 v63, 0x43800000, v63
	v_mul_f32_e32 v69, 0x43800000, v69
	v_mul_f32_e32 v71, 0x43800000, v71
	v_mul_f32_e32 v77, 0x43800000, v77
	v_mul_f32_e32 v79, 0x43800000, v79
	v_mul_f32_e32 v85, 0x43800000, v85
	v_mul_f32_e32 v87, 0x43800000, v87
	v_cvt_pk_fp8_f32 v2, v60, v62
	v_cvt_pk_fp8_f32 v3, v68, v70
	v_cvt_pk_fp8_f32 v4, v76, v78
	v_cvt_pk_fp8_f32 v5, v84, v86
	v_mov_b32_e32 v10, 0
	v_mov_b32_e32 v11, 0
	v_mov_b32_e32 v12, 0
	v_mov_b32_e32 v13, 0
	s_and_b32 s9, s9, 0xffffff80
	s_lshl_b32 s14, s14, 1
	s_sext_i32_i16 s8, s8
	v_mul_f32_e32 v92, 0x43800000, v92
	v_mul_f32_e32 v94, 0x43800000, v94
	s_waitcnt lgkmcnt(11)
; #define LAS __attribute__((address_space(3)))
; #define LDS_WAIT() asm volatile("s_waitcnt lgkmcnt(0)" ::: "memory")
; #define MOE_LOAD(r_, RG) do { int rr_ = (r_); \
;         if (rr_ < 65536) { const int e_ = rr_ / 2048, q_ = rr_ % 2048; item8_load(w_gu + (size_t)e_ * 2048 * 4096, 4096, 128 * (q_ / 128), 32 * (q_ % 128), lane, RG); } \
;         else { rr_ -= 65536; const int e_ = rr_ / 1024, q_ = rr_ % 1024; item8_load(w_dn + (size_t)e_ * 2048 * 2048, D, 128 * (q_ / 64), 32 * (q_ % 64), lane, RG); } } while (0)
; __device__ __forceinline__ void item8_finish(int K, unsigned char* WT, int k0, int r0, LAS float* scr, int lane, const f32x4 (&rg)[16]) {
; #pragma unroll
;     for (int i = 0; i < 16; ++i) { LAS float* d = scr + (8 * i + (lane >> 3)) * 33 + 4 * (lane & 7); d[0] = rg[i].x; d[1] = rg[i].y; d[2] = rg[i].z; d[3] = rg[i].w; }
;     LDS_WAIT();
;     const int c = lane & 7;
; #pragma unroll
;     for (int j = 0; j < 4; ++j) { const int n = (lane >> 3) + 8 * j; const LAS float* sp = scr + (16 * c) * 33 + n; int w[4];
; #pragma unroll
;         for (int q = 0; q < 4; ++q) { w[q] = __builtin_amdgcn_cvt_pk_fp8_f32(sp[(4 * q) * 33] * 256.f, sp[(4 * q + 1) * 33] * 256.f, 0, false); w[q] = __builtin_amdgcn_cvt_pk_fp8_f32(sp[(4 * q + 2) * 33] * 256.f, sp[(4 * q + 3) * 33] * 256.f, w[q], true); }
;         u32x4 o; o.x = (unsigned)w[0]; o.y = (unsigned)w[1]; o.z = (unsigned)w[2]; o.w = (unsigned)w[3];
;         __builtin_nontemporal_store(o, (u32x4*)(WT + (size_t)(r0 + n) * K + k0 + 16 * c)); }
;     LDS_WAIT();
; }
; __global__ void __launch_bounds__(NTHREADS, 2) fwd(Args args) {
;     ...
;         if (bid >= 64) for (int sl_ = (bid - 64) * 7 + wave - 1; sl_ < CVSK; sl_ += (G - 64) * 7) { const int it_ = CV_P0 - CVBG - CVSK + sl_; f32x4 rg_[16]; MOE_LOAD(it_, rg_); MOE_FIN(it_, rg_); } });
	v_mul_f32_e32 v100, 0x43800000, v100
	s_waitcnt lgkmcnt(10)
	v_mul_f32_e32 v102, 0x43800000, v102
	s_waitcnt lgkmcnt(7)
	v_mul_f32_e32 v108, 0x43800000, v108
	s_waitcnt lgkmcnt(6)
	v_mul_f32_e32 v110, 0x43800000, v110
	s_waitcnt lgkmcnt(3)
	v_mul_f32_e32 v116, 0x43800000, v116
	s_waitcnt lgkmcnt(2)
	v_mul_f32_e32 v118, 0x43800000, v118
	v_cvt_pk_fp8_f32 v6, v61, v63
	v_cvt_pk_fp8_f32 v7, v69, v71
	v_cvt_pk_fp8_f32 v8, v77, v79
	v_cvt_pk_fp8_f32 v9, v85, v87
	v_mov_b32_e32 v14, 0
	v_mov_b32_e32 v15, 0
	v_mov_b32_e32 v16, 0
	v_mov_b32_e32 v17, 0
	s_and_b32 s12, s14, 0xffffff00
	s_add_i32 s8, s9, s8
	v_mul_f32_e32 v93, 0x43800000, v93
	v_mul_f32_e32 v95, 0x43800000, v95
	v_mul_f32_e32 v101, 0x43800000, v101
	v_mul_f32_e32 v103, 0x43800000, v103
	v_mul_f32_e32 v109, 0x43800000, v109
	v_mul_f32_e32 v111, 0x43800000, v111
	v_mul_f32_e32 v117, 0x43800000, v117
	v_mul_f32_e32 v119, 0x43800000, v119
	v_cvt_pk_fp8_f32 v10, v92, v94
	v_cvt_pk_fp8_f32 v11, v100, v102
	v_cvt_pk_fp8_f32 v12, v108, v110
	v_cvt_pk_fp8_f32 v13, v116, v118
	s_ashr_i32 s13, s16, 31
	s_add_i32 s9, s8, s12
	v_mul_f32_e32 v64, 0x43800000, v64
	v_mul_f32_e32 v66, 0x43800000, v66
	v_mul_f32_e32 v72, 0x43800000, v72
	v_mul_f32_e32 v74, 0x43800000, v74
	v_mul_f32_e32 v80, 0x43800000, v80
	v_mul_f32_e32 v82, 0x43800000, v82
	v_mul_f32_e32 v88, 0x43800000, v88
	v_mul_f32_e32 v90, 0x43800000, v90
	v_cvt_pk_fp8_f32 v14, v93, v95
	v_cvt_pk_fp8_f32 v15, v101, v103
	v_cvt_pk_fp8_f32 v16, v109, v111
	v_cvt_pk_fp8_f32 v17, v117, v119
	s_add_u32 s8, s10, s16
	v_add_u32_e32 v124, s9, v22
	v_mul_f32_e32 v65, 0x43800000, v65
	v_mul_f32_e32 v67, 0x43800000, v67
	v_mul_f32_e32 v73, 0x43800000, v73
	v_mul_f32_e32 v75, 0x43800000, v75
	v_mul_f32_e32 v81, 0x43800000, v81
	v_mul_f32_e32 v83, 0x43800000, v83
	v_mul_f32_e32 v89, 0x43800000, v89
	v_mul_f32_e32 v91, 0x43800000, v91
	v_cvt_pk_fp8_f32 v2, v64, v66 op_sel:[0,0,1]
	v_cvt_pk_fp8_f32 v3, v72, v74 op_sel:[0,0,1]
	v_cvt_pk_fp8_f32 v4, v80, v82 op_sel:[0,0,1]
	v_cvt_pk_fp8_f32 v5, v88, v90 op_sel:[0,0,1]
	v_add_u32_e32 v126, s9, v23
	v_add_u32_e32 v128, s9, v24
	v_add_u32_e32 v130, s9, v25
	s_addc_u32 s9, s11, s13
	v_ashrrev_i32_e32 v125, 31, v124
	v_mul_f32_e32 v96, 0x43800000, v96
	v_mul_f32_e32 v98, 0x43800000, v98
	v_mul_f32_e32 v104, 0x43800000, v104
	v_mul_f32_e32 v106, 0x43800000, v106
	v_mul_f32_e32 v112, 0x43800000, v112
	v_mul_f32_e32 v114, 0x43800000, v114
	s_waitcnt lgkmcnt(1)
	v_mul_f32_e32 v120, 0x43800000, v120
	s_waitcnt lgkmcnt(0)
	v_mul_f32_e32 v122, 0x43800000, v122
	v_cvt_pk_fp8_f32 v6, v65, v67 op_sel:[0,0,1]
	v_cvt_pk_fp8_f32 v7, v73, v75 op_sel:[0,0,1]
	v_cvt_pk_fp8_f32 v8, v81, v83 op_sel:[0,0,1]
	v_cvt_pk_fp8_f32 v9, v89, v91 op_sel:[0,0,1]
	v_ashrrev_i32_e32 v127, 31, v126
	v_ashrrev_i32_e32 v129, 31, v128
	v_ashrrev_i32_e32 v131, 31, v130
	v_lshl_add_u64 v[132:133], s[8:9], 0, v[18:19]
	v_lshlrev_b64 v[124:125], 11, v[124:125]
	v_mul_f32_e32 v97, 0x43800000, v97
	v_mul_f32_e32 v99, 0x43800000, v99
	v_mul_f32_e32 v105, 0x43800000, v105
	v_mul_f32_e32 v107, 0x43800000, v107
	v_mul_f32_e32 v113, 0x43800000, v113
	v_mul_f32_e32 v115, 0x43800000, v115
	v_mul_f32_e32 v121, 0x43800000, v121
	v_mul_f32_e32 v123, 0x43800000, v123
	v_cvt_pk_fp8_f32 v10, v96, v98 op_sel:[0,0,1]
	v_cvt_pk_fp8_f32 v11, v104, v106 op_sel:[0,0,1]
	v_cvt_pk_fp8_f32 v12, v112, v114 op_sel:[0,0,1]
	v_cvt_pk_fp8_f32 v13, v120, v122 op_sel:[0,0,1]
	v_lshlrev_b64 v[126:127], 11, v[126:127]
	v_lshlrev_b64 v[128:129], 11, v[128:129]
	v_lshlrev_b64 v[130:131], 11, v[130:131]
	v_lshl_add_u64 v[124:125], v[132:133], 0, v[124:125]
	v_cvt_pk_fp8_f32 v14, v97, v99 op_sel:[0,0,1]
	v_cvt_pk_fp8_f32 v15, v105, v107 op_sel:[0,0,1]
	v_cvt_pk_fp8_f32 v16, v113, v115 op_sel:[0,0,1]
	v_cvt_pk_fp8_f32 v17, v121, v123 op_sel:[0,0,1]
	v_lshl_add_u64 v[126:127], v[132:133], 0, v[126:127]
	v_lshl_add_u64 v[128:129], v[132:133], 0, v[128:129]
	v_lshl_add_u64 v[130:131], v[132:133], 0, v[130:131]
	global_store_dwordx4 v[124:125], v[2:5], off nt
	global_store_dwordx4 v[126:127], v[6:9], off nt
	global_store_dwordx4 v[128:129], v[10:13], off nt
	global_store_dwordx4 v[130:131], v[14:17], off nt
	s_waitcnt lgkmcnt(0)
	s_add_i32 s2, s2, s3
	s_cmpk_lt_i32 s2, 0xfc0
	s_cbranch_scc1 .LBB0_379
